# P7 prologue: product-key f32->bf16 LDS image loads fully unrolled (16 loads in flight, one round trip instead of four)
# baseline (speedup 1.0000x reference)
; #define GAS __attribute__((address_space(1)))
; #define LAS __attribute__((address_space(3)))
; DI unsigned pk2(float lo, float hi) { return f2bf(lo) | (f2bf(hi) << 16); }
; DI void p8_phase(Frame& F) {
;     ...
; #pragma unroll 4
;     for (int i = 0; i < 16; ++i) { const int idx = tid * 4 + 2048 * i, side = idx >> 14, rem = idx & 16383, row = rem >> 7, col = rem & 127;
;         const f32x4 a = *(const GAS f32x4*)((side ? F.keys2 : F.keys1) + rem);
;         v2u o; o.x = pk2(a.x, a.y); o.y = pk2(a.z, a.w); *(LAS v2u*)(KIMG + (side * 128 + row) * KPITCH + col * 2) = o; }
.LBB0_1201:
	v_readlane_b32 s4, v252, 4
	v_readlane_b32 s5, v252, 5
	s_cmp_lt_i32 s4, 9
	v_readlane_b32 s4, v252, 13
	s_cselect_b64 s[2:3], -1, 0
	v_readlane_b32 s5, v252, 14
	s_add_u32 s14, s4, 0x3400000
	s_addc_u32 s15, s5, 0
	s_add_u32 s16, s4, 0x2c00000
	s_addc_u32 s17, s5, 0
	s_add_u32 s37, s4, 0x18000000
	s_addc_u32 s39, s5, 0
	s_add_u32 s18, s4, 0x1a000000
	s_addc_u32 s19, s5, 0
	s_add_u32 s20, s4, 0x380000
	s_addc_u32 s21, s5, 0
	s_add_u32 s24, s4, 0x390000
	s_addc_u32 s25, s5, 0
	s_and_b64 s[8:9], s[2:3], s[0:1]
	s_andn2_b64 vcc, exec, s[8:9]
	v_readlane_b32 s6, v252, 6
	v_readlane_b32 s7, v252, 7
	s_cbranch_vccnz .LBB0_1246
	v_lshlrev_b32_e32 v1, 3, v0
	v_lshrrev_b32_e32 v3, 5, v0
	s_waitcnt lgkmcnt(0)
	v_and_b32_e32 v2, 0xf8, v1
	v_or_b32_e32 v1, 48, v3
	v_or_b32_e32 v4, 32, v3
	v_or_b32_e32 v5, 16, v3
	v_mul_u32_u24_e32 v1, 0x110, v1
	v_mul_u32_u24_e32 v4, 0x110, v4
	v_mul_u32_u24_e32 v5, 0x110, v5
	v_mul_u32_u24_e32 v3, 0x110, v3
	s_mov_b32 s2, 0
	v_add3_u32 v1, v1, v2, 0
	v_add3_u32 v4, v4, v2, 0
	v_add3_u32 v5, v5, v2, 0
	v_add3_u32 v6, v3, v2, 0
	s_movk_i32 s3, 0x7fff
	s_mov_b32 s4, 0xffff0000
	s_movk_i32 s5, 0x4000
	v_mov_b32_e32 v7, s79
	s_waitcnt vmcnt(31)
	v_mov_b32_e32 v8, s77
	s_waitcnt vmcnt(30)
	v_mov_b32_e32 v9, s78
	v_mov_b32_e32 v10, s76
	v_mov_b32_e32 v3, 0
	s_mov_b32 s6, 0
	v_add_u32_e32 v2, s2, v150
	s_cmp_lt_u32 s6, 8
	v_and_b32_e32 v11, 0x2ffc, v2
	v_add_u32_e32 v40, 0x800, v2
	v_add_u32_e32 v41, 0x1000, v2
	s_cselect_b32 s11, s77, s79
	s_cselect_b32 s10, s76, s78
	s_cmpk_lt_u32 s2, 0x4000
	v_add_u32_e32 v2, 0x1800, v2
	v_lshlrev_b32_e32 v11, 2, v11
	v_and_b32_e32 v44, 0x3ffc, v40
	v_cmp_gt_u32_e32 vcc, s5, v40
	v_and_b32_e32 v45, 0x3ffc, v41
	s_cselect_b32 s13, s77, s79
	v_cndmask_b32_e32 v49, v7, v8, vcc
	s_cselect_b32 s12, s76, s78
	v_and_b32_e32 v50, 0x3ffc, v2
	v_cmp_gt_u32_e64 s[0:1], s5, v2
	global_load_dwordx4 v[40:43], v11, s[10:11]
	v_cndmask_b32_e32 v48, v9, v10, vcc
	v_lshlrev_b32_e32 v2, 2, v44
	v_lshlrev_b32_e32 v11, 2, v45
	v_cndmask_b32_e64 v53, v7, v8, s[0:1]
	v_cndmask_b32_e64 v52, v9, v10, s[0:1]
	global_load_dwordx4 v[44:47], v11, s[12:13]
	v_lshl_add_u64 v[48:49], v[48:49], 0, v[2:3]
	v_lshlrev_b32_e32 v2, 2, v50
	global_load_dwordx4 v[48:51], v[48:49], off
	v_lshl_add_u64 v[52:53], v[52:53], 0, v[2:3]
	global_load_dwordx4 v[52:55], v[52:53], off
	s_add_i32 s6, s6, 4
	s_addk_i32 s2, 0x2000
	s_cmpk_eq_u32 s2, 0x8000
	v_add_u32_e32 v2, s2, v150
	s_cmp_lt_u32 s6, 8
	v_and_b32_e32 v11, 0x2ffc, v2
	v_add_u32_e32 v56, 0x800, v2
	v_add_u32_e32 v57, 0x1000, v2
	s_cselect_b32 s11, s77, s79
	s_cselect_b32 s10, s76, s78
	s_cmpk_lt_u32 s2, 0x4000
	v_add_u32_e32 v2, 0x1800, v2
	v_lshlrev_b32_e32 v11, 2, v11
	v_and_b32_e32 v60, 0x3ffc, v56
	v_cmp_gt_u32_e32 vcc, s5, v56
	v_and_b32_e32 v61, 0x3ffc, v57
	s_cselect_b32 s13, s77, s79
	v_cndmask_b32_e32 v65, v7, v8, vcc
	s_cselect_b32 s12, s76, s78
	v_and_b32_e32 v66, 0x3ffc, v2
	v_cmp_gt_u32_e64 s[0:1], s5, v2
	global_load_dwordx4 v[56:59], v11, s[10:11]
	v_cndmask_b32_e32 v64, v9, v10, vcc
	v_lshlrev_b32_e32 v2, 2, v60
	v_lshlrev_b32_e32 v11, 2, v61
	v_cndmask_b32_e64 v69, v7, v8, s[0:1]
	v_cndmask_b32_e64 v68, v9, v10, s[0:1]
	global_load_dwordx4 v[60:63], v11, s[12:13]
	v_lshl_add_u64 v[64:65], v[64:65], 0, v[2:3]
	v_lshlrev_b32_e32 v2, 2, v66
	global_load_dwordx4 v[64:67], v[64:65], off
	v_lshl_add_u64 v[68:69], v[68:69], 0, v[2:3]
	global_load_dwordx4 v[68:71], v[68:69], off
	s_add_i32 s6, s6, 4
	s_addk_i32 s2, 0x2000
	s_cmpk_eq_u32 s2, 0x8000
	v_add_u32_e32 v2, s2, v150
	s_cmp_lt_u32 s6, 8
	v_and_b32_e32 v11, 0x2ffc, v2
	v_add_u32_e32 v72, 0x800, v2
	v_add_u32_e32 v73, 0x1000, v2
	s_cselect_b32 s11, s77, s79
	s_cselect_b32 s10, s76, s78
	s_cmpk_lt_u32 s2, 0x4000
	v_add_u32_e32 v2, 0x1800, v2
	v_lshlrev_b32_e32 v11, 2, v11
	v_and_b32_e32 v76, 0x3ffc, v72
	v_cmp_gt_u32_e32 vcc, s5, v72
	v_and_b32_e32 v77, 0x3ffc, v73
	s_cselect_b32 s13, s77, s79
	v_cndmask_b32_e32 v81, v7, v8, vcc
	s_cselect_b32 s12, s76, s78
	v_and_b32_e32 v82, 0x3ffc, v2
	v_cmp_gt_u32_e64 s[0:1], s5, v2
	global_load_dwordx4 v[72:75], v11, s[10:11]
	v_cndmask_b32_e32 v80, v9, v10, vcc
	v_lshlrev_b32_e32 v2, 2, v76
	v_lshlrev_b32_e32 v11, 2, v77
	v_cndmask_b32_e64 v85, v7, v8, s[0:1]
	v_cndmask_b32_e64 v84, v9, v10, s[0:1]
	global_load_dwordx4 v[76:79], v11, s[12:13]
	v_lshl_add_u64 v[80:81], v[80:81], 0, v[2:3]
	v_lshlrev_b32_e32 v2, 2, v82
	global_load_dwordx4 v[80:83], v[80:81], off
	v_lshl_add_u64 v[84:85], v[84:85], 0, v[2:3]
	global_load_dwordx4 v[84:87], v[84:85], off
	s_add_i32 s6, s6, 4
	s_addk_i32 s2, 0x2000
	s_cmpk_eq_u32 s2, 0x8000
	v_add_u32_e32 v2, s2, v150
	s_cmp_lt_u32 s6, 8
	v_and_b32_e32 v11, 0x2ffc, v2
	v_add_u32_e32 v88, 0x800, v2
	v_add_u32_e32 v89, 0x1000, v2
	s_cselect_b32 s11, s77, s79
	s_cselect_b32 s10, s76, s78
	s_cmpk_lt_u32 s2, 0x4000
	v_add_u32_e32 v2, 0x1800, v2
	v_lshlrev_b32_e32 v11, 2, v11
	v_and_b32_e32 v92, 0x3ffc, v88
	v_cmp_gt_u32_e32 vcc, s5, v88
	v_and_b32_e32 v93, 0x3ffc, v89
	s_cselect_b32 s13, s77, s79
	v_cndmask_b32_e32 v97, v7, v8, vcc
	s_cselect_b32 s12, s76, s78
	v_and_b32_e32 v98, 0x3ffc, v2
	v_cmp_gt_u32_e64 s[0:1], s5, v2
	global_load_dwordx4 v[88:91], v11, s[10:11]
	v_cndmask_b32_e32 v96, v9, v10, vcc
	v_lshlrev_b32_e32 v2, 2, v92
	v_lshlrev_b32_e32 v11, 2, v93
	v_cndmask_b32_e64 v101, v7, v8, s[0:1]
	v_cndmask_b32_e64 v100, v9, v10, s[0:1]
	global_load_dwordx4 v[92:95], v11, s[12:13]
	v_lshl_add_u64 v[96:97], v[96:97], 0, v[2:3]
	v_lshlrev_b32_e32 v2, 2, v98
	global_load_dwordx4 v[96:99], v[96:97], off
	v_lshl_add_u64 v[100:101], v[100:101], 0, v[2:3]
	global_load_dwordx4 v[100:103], v[100:101], off
	s_add_i32 s6, s6, 4
	s_addk_i32 s2, 0x2000
	s_cmpk_eq_u32 s2, 0x8000
	s_waitcnt vmcnt(15)
; #define GAS __attribute__((address_space(1)))
; #define LAS __attribute__((address_space(3)))
; DI unsigned f2bf(float f) { unsigned u = __builtin_bit_cast(unsigned, f); return (u + 0x7fffu + ((u >> 16) & 1u)) >> 16; }
; DI unsigned pk2(float lo, float hi) { return f2bf(lo) | (f2bf(hi) << 16); }
; DI void p8_phase(Frame& F) {
;     ...
; #pragma unroll 4
;     for (int i = 0; i < 16; ++i) { const int idx = tid * 4 + 2048 * i, side = idx >> 14, rem = idx & 16383, row = rem >> 7, col = rem & 127;
;         const f32x4 a = *(const GAS f32x4*)((side ? F.keys2 : F.keys1) + rem);
;         v2u o; o.x = pk2(a.x, a.y); o.y = pk2(a.z, a.w); *(LAS v2u*)(KIMG + (side * 128 + row) * KPITCH + col * 2) = o; }
;     __syncthreads();
	v_bfe_u32 v2, v40, 16, 1
	v_bfe_u32 v28, v42, 16, 1
	v_bfe_u32 v11, v41, 16, 1
	v_bfe_u32 v29, v43, 16, 1
	v_add3_u32 v2, v40, v2, s3
	v_add3_u32 v40, v42, v28, s3
	s_waitcnt vmcnt(14)
	v_bfe_u32 v42, v44, 16, 1
	v_bfe_u32 v28, v46, 16, 1
	v_add3_u32 v11, v41, v11, s3
	v_add3_u32 v41, v43, v29, s3
	v_bfe_u32 v43, v45, 16, 1
	v_bfe_u32 v29, v47, 16, 1
	v_lshrrev_b32_e32 v2, 16, v2
	v_lshrrev_b32_e32 v30, 16, v40
	s_waitcnt vmcnt(13)
	v_bfe_u32 v31, v48, 16, 1
	v_bfe_u32 v33, v50, 16, 1
	v_add3_u32 v42, v44, v42, s3
	v_add3_u32 v44, v46, v28, s3
	v_bfe_u32 v32, v49, 16, 1
	v_bfe_u32 v34, v51, 16, 1
	v_add3_u32 v43, v45, v43, s3
	v_add3_u32 v45, v47, v29, s3
	v_and_or_b32 v40, v11, s4, v2
	v_and_or_b32 v41, v41, s4, v30
	v_add3_u32 v2, v48, v31, s3
	v_add3_u32 v46, v50, v33, s3
	v_lshrrev_b32_e32 v44, 16, v44
	s_waitcnt vmcnt(12)
	v_bfe_u32 v48, v52, 16, 1
	v_bfe_u32 v50, v54, 16, 1
	v_add3_u32 v11, v49, v32, s3
	v_add3_u32 v47, v51, v34, s3
	v_lshrrev_b32_e32 v42, 16, v42
	v_bfe_u32 v49, v53, 16, 1
	v_bfe_u32 v51, v55, 16, 1
	ds_write_b64 v6, v[40:41]
	v_lshrrev_b32_e32 v2, 16, v2
	v_lshrrev_b32_e32 v46, 16, v46
	v_and_or_b32 v41, v45, s4, v44
	v_add3_u32 v44, v52, v48, s3
	v_add3_u32 v48, v54, v50, s3
	v_and_or_b32 v40, v43, s4, v42
	v_add3_u32 v45, v53, v49, s3
	v_add3_u32 v49, v55, v51, s3
	v_and_or_b32 v42, v11, s4, v2
	v_and_or_b32 v43, v47, s4, v46
	v_lshrrev_b32_e32 v2, 16, v44
	v_lshrrev_b32_e32 v11, 16, v48
	ds_write_b64 v5, v[42:43]
	ds_write_b64 v4, v[40:41]
	v_and_or_b32 v40, v45, s4, v2
	v_and_or_b32 v41, v49, s4, v11
	ds_write_b64 v1, v[40:41]
	s_waitcnt vmcnt(11)
	v_bfe_u32 v2, v56, 16, 1
	v_bfe_u32 v28, v58, 16, 1
	v_bfe_u32 v11, v57, 16, 1
	v_bfe_u32 v29, v59, 16, 1
	v_add3_u32 v2, v56, v2, s3
	v_add3_u32 v56, v58, v28, s3
	s_waitcnt vmcnt(10)
	v_bfe_u32 v58, v60, 16, 1
	v_bfe_u32 v28, v62, 16, 1
	v_add3_u32 v11, v57, v11, s3
	v_add3_u32 v57, v59, v29, s3
	v_bfe_u32 v59, v61, 16, 1
	v_bfe_u32 v29, v63, 16, 1
	v_lshrrev_b32_e32 v2, 16, v2
	v_lshrrev_b32_e32 v30, 16, v56
	s_waitcnt vmcnt(9)
	v_bfe_u32 v31, v64, 16, 1
	v_bfe_u32 v33, v66, 16, 1
	v_add3_u32 v58, v60, v58, s3
	v_add3_u32 v60, v62, v28, s3
	v_bfe_u32 v32, v65, 16, 1
	v_bfe_u32 v34, v67, 16, 1
	v_add3_u32 v59, v61, v59, s3
	v_add3_u32 v61, v63, v29, s3
	v_and_or_b32 v56, v11, s4, v2
	v_and_or_b32 v57, v57, s4, v30
	v_add3_u32 v2, v64, v31, s3
	v_add3_u32 v62, v66, v33, s3
	v_lshrrev_b32_e32 v60, 16, v60
	s_waitcnt vmcnt(8)
	v_bfe_u32 v64, v68, 16, 1
	v_bfe_u32 v66, v70, 16, 1
	v_add3_u32 v11, v65, v32, s3
	v_add3_u32 v63, v67, v34, s3
	v_lshrrev_b32_e32 v58, 16, v58
	v_bfe_u32 v65, v69, 16, 1
	v_bfe_u32 v67, v71, 16, 1
	ds_write_b64 v6, v[56:57] offset:17408
	v_lshrrev_b32_e32 v2, 16, v2
	v_lshrrev_b32_e32 v62, 16, v62
	v_and_or_b32 v57, v61, s4, v60
	v_add3_u32 v60, v68, v64, s3
	v_add3_u32 v64, v70, v66, s3
	v_and_or_b32 v56, v59, s4, v58
	v_add3_u32 v61, v69, v65, s3
	v_add3_u32 v65, v71, v67, s3
	v_and_or_b32 v58, v11, s4, v2
	v_and_or_b32 v59, v63, s4, v62
	v_lshrrev_b32_e32 v2, 16, v60
	v_lshrrev_b32_e32 v11, 16, v64
	ds_write_b64 v5, v[58:59] offset:17408
	ds_write_b64 v4, v[56:57] offset:17408
	v_and_or_b32 v56, v61, s4, v2
	v_and_or_b32 v57, v65, s4, v11
	ds_write_b64 v1, v[56:57] offset:17408
	s_waitcnt vmcnt(7)
	v_bfe_u32 v2, v72, 16, 1
	v_bfe_u32 v28, v74, 16, 1
	v_bfe_u32 v11, v73, 16, 1
	v_bfe_u32 v29, v75, 16, 1
	v_add3_u32 v2, v72, v2, s3
	v_add3_u32 v72, v74, v28, s3
	s_waitcnt vmcnt(6)
	v_bfe_u32 v74, v76, 16, 1
	v_bfe_u32 v28, v78, 16, 1
	v_add3_u32 v11, v73, v11, s3
	v_add3_u32 v73, v75, v29, s3
	v_bfe_u32 v75, v77, 16, 1
	v_bfe_u32 v29, v79, 16, 1
	v_lshrrev_b32_e32 v2, 16, v2
	v_lshrrev_b32_e32 v30, 16, v72
	s_waitcnt vmcnt(5)
	v_bfe_u32 v31, v80, 16, 1
	v_bfe_u32 v33, v82, 16, 1
	v_add3_u32 v74, v76, v74, s3
	v_add3_u32 v76, v78, v28, s3
	v_bfe_u32 v32, v81, 16, 1
	v_bfe_u32 v34, v83, 16, 1
	v_add3_u32 v75, v77, v75, s3
	v_add3_u32 v77, v79, v29, s3
	v_and_or_b32 v72, v11, s4, v2
	v_and_or_b32 v73, v73, s4, v30
	v_add3_u32 v2, v80, v31, s3
	v_add3_u32 v78, v82, v33, s3
	v_lshrrev_b32_e32 v76, 16, v76
	s_waitcnt vmcnt(4)
	v_bfe_u32 v80, v84, 16, 1
	v_bfe_u32 v82, v86, 16, 1
	v_add3_u32 v11, v81, v32, s3
	v_add3_u32 v79, v83, v34, s3
	v_lshrrev_b32_e32 v74, 16, v74
	v_bfe_u32 v81, v85, 16, 1
	v_bfe_u32 v83, v87, 16, 1
	ds_write_b64 v6, v[72:73] offset:34816
	v_lshrrev_b32_e32 v2, 16, v2
	v_lshrrev_b32_e32 v78, 16, v78
	v_and_or_b32 v73, v77, s4, v76
	v_add3_u32 v76, v84, v80, s3
	v_add3_u32 v80, v86, v82, s3
	v_and_or_b32 v72, v75, s4, v74
	v_add3_u32 v77, v85, v81, s3
	v_add3_u32 v81, v87, v83, s3
	v_and_or_b32 v74, v11, s4, v2
	v_and_or_b32 v75, v79, s4, v78
	v_lshrrev_b32_e32 v2, 16, v76
	v_lshrrev_b32_e32 v11, 16, v80
	ds_write_b64 v5, v[74:75] offset:34816
	ds_write_b64 v4, v[72:73] offset:34816
	v_and_or_b32 v72, v77, s4, v2
	v_and_or_b32 v73, v81, s4, v11
	ds_write_b64 v1, v[72:73] offset:34816
	s_waitcnt vmcnt(3)
	v_bfe_u32 v2, v88, 16, 1
	v_bfe_u32 v28, v90, 16, 1
	v_bfe_u32 v11, v89, 16, 1
	v_bfe_u32 v29, v91, 16, 1
	v_add3_u32 v2, v88, v2, s3
	v_add3_u32 v88, v90, v28, s3
	s_waitcnt vmcnt(2)
	v_bfe_u32 v90, v92, 16, 1
	v_bfe_u32 v28, v94, 16, 1
	v_add3_u32 v11, v89, v11, s3
	v_add3_u32 v89, v91, v29, s3
	v_bfe_u32 v91, v93, 16, 1
	v_bfe_u32 v29, v95, 16, 1
	v_lshrrev_b32_e32 v2, 16, v2
	v_lshrrev_b32_e32 v30, 16, v88
	s_waitcnt vmcnt(1)
	v_bfe_u32 v31, v96, 16, 1
	v_bfe_u32 v33, v98, 16, 1
	v_add3_u32 v90, v92, v90, s3
	v_add3_u32 v92, v94, v28, s3
	v_bfe_u32 v32, v97, 16, 1
	v_bfe_u32 v34, v99, 16, 1
	v_add3_u32 v91, v93, v91, s3
	v_add3_u32 v93, v95, v29, s3
	v_and_or_b32 v88, v11, s4, v2
	v_and_or_b32 v89, v89, s4, v30
	v_add3_u32 v2, v96, v31, s3
	v_add3_u32 v94, v98, v33, s3
	v_lshrrev_b32_e32 v92, 16, v92
	s_waitcnt vmcnt(0)
	v_bfe_u32 v96, v100, 16, 1
	v_bfe_u32 v98, v102, 16, 1
	v_add3_u32 v11, v97, v32, s3
	v_add3_u32 v95, v99, v34, s3
	v_lshrrev_b32_e32 v90, 16, v90
	v_bfe_u32 v97, v101, 16, 1
	v_bfe_u32 v99, v103, 16, 1
	ds_write_b64 v6, v[88:89] offset:52224
	v_lshrrev_b32_e32 v2, 16, v2
	v_lshrrev_b32_e32 v94, 16, v94
	v_and_or_b32 v89, v93, s4, v92
	v_add3_u32 v92, v100, v96, s3
	v_add3_u32 v96, v102, v98, s3
	v_and_or_b32 v88, v91, s4, v90
	v_add3_u32 v93, v101, v97, s3
	v_add3_u32 v97, v103, v99, s3
	v_and_or_b32 v90, v11, s4, v2
	v_and_or_b32 v91, v95, s4, v94
	v_lshrrev_b32_e32 v2, 16, v92
	v_lshrrev_b32_e32 v11, 16, v96
	ds_write_b64 v5, v[90:91] offset:52224
	ds_write_b64 v4, v[88:89] offset:52224
	v_and_or_b32 v88, v93, s4, v2
	v_and_or_b32 v89, v97, s4, v11
	ds_write_b64 v1, v[88:89] offset:52224
	v_add_u32_e32 v6, 0x11000, v6
	v_add_u32_e32 v4, 0x11000, v4
	v_add_u32_e32 v5, 0x11000, v5
	v_add_u32_e32 v1, 0x11000, v1
	v_readlane_b32 s0, v252, 12
	s_lshl_b32 s35, s0, 3
	v_readlane_b32 s0, v252, 11
	s_lshl_b32 s34, s0, 3
	s_andn2_b64 vcc, exec, s[22:23]
	s_mov_b32 s10, 0
	s_waitcnt lgkmcnt(0)
	s_barrier
; #define GAS __attribute__((address_space(1)))
; #define LAS __attribute__((address_space(3)))
; DI unsigned pk2(float lo, float hi) { return f2bf(lo) | (f2bf(hi) << 16); }
; DI int crow(int reg, int h) { return (reg & 3) + 8 * (reg >> 2) + 4 * h; }
; DI void p8_phase(Frame& F) {
;     LAS unsigned char* KIMG = F.lds; LAS unsigned char* TBL = F.lds + P8_TBL + F.wave * 1024;
;     const int lane = F.lane, tid = F.tid, r = lane & 31, h = lane >> 5;
; #pragma unroll 4
;     for (int i = 0; i < 16; ++i) { const int idx = tid * 4 + 2048 * i, side = idx >> 14, rem = idx & 16383, row = rem >> 7, col = rem & 127;
;         const f32x4 a = *(const GAS f32x4*)((side ? F.keys2 : F.keys1) + rem);
;         v2u o; o.x = pk2(a.x, a.y); o.y = pk2(a.z, a.w); *(LAS v2u*)(KIMG + (side * 128 + row) * KPITCH + col * 2) = o; }
;     __syncthreads();
;     const int gcT = F.vcu * NWAVES + F.wave, NGWT = F.G * NWAVES; int trow_it = 0;
;     for (int it = (int)blockIdx.x; it < (M / 256) * PH; it += F.G, ++trow_it) {
;         const int tile = it / PH, hd = it % PH;
;         const int t = tile * 256 + F.wave * 32 + r;
;     ...
;                 for (int reg = 0; reg < 16; ++reg) { const unsigned key = (unsigned)(kt * 32 + crow(reg, h)); const float sv = acc[kt][reg];
	s_cbranch_vccnz .LBB0_1237
	v_mbcnt_hi_u32_b32 v1, -1, v200
	v_and_b32_e32 v3, 64, v1
	v_xor_b32_e32 v2, 32, v1
	v_add_u32_e32 v3, 64, v3
	s_lshl_b32 s0, s89, 10
	v_cmp_lt_i32_e32 vcc, v2, v3
	s_add_i32 s0, s0, 0
	s_add_i32 s2, s0, 0x11000
	v_cndmask_b32_e32 v1, v1, v2, vcc
	v_lshlrev_b32_e32 v130, 3, v197
	v_lshlrev_b32_e32 v131, 2, v197
	v_lshlrev_b32_e32 v137, 2, v1
	v_lshlrev_b32_e32 v1, 5, v148
	s_add_i32 s36, s35, s89
	s_mov_b32 s11, 0
	v_mov_b32_e32 v133, 0
	v_cmp_gt_u32_e64 s[0:1], 32, v148
	v_cmp_lt_u32_e64 s[6:7], 31, v148
	v_lshl_add_u32 v139, v149, 5, s2
	v_lshl_add_u32 v144, v197, 4, 0
	v_lshl_or_b32 v145, s89, 5, v149
	v_cmp_eq_u32_e64 s[4:5], 0, v148
	v_or_b32_e32 v147, 1, v131
	v_or_b32_e32 v151, 2, v131
	v_or_b32_e32 v152, 3, v131
	v_or_b32_e32 v153, 8, v131
	v_or_b32_e32 v154, 9, v131
	v_or_b32_e32 v155, 10, v131
	v_or_b32_e32 v156, 11, v131
	v_or_b32_e32 v157, 16, v131
	v_or_b32_e32 v158, 17, v131
	v_or_b32_e32 v159, 18, v131
	v_or_b32_e32 v160, 19, v131
	v_or_b32_e32 v161, 24, v131
	v_or_b32_e32 v162, 25, v131
	v_or_b32_e32 v163, 26, v131
	v_or_b32_e32 v164, 27, v131
	v_or_b32_e32 v165, 32, v131
	v_or_b32_e32 v166, 33, v131
	v_or_b32_e32 v167, 34, v131
	v_or_b32_e32 v168, 35, v131
	v_or_b32_e32 v169, 40, v131
	v_or_b32_e32 v170, 41, v131
	v_or_b32_e32 v171, 42, v131
	v_or_b32_e32 v172, 43, v131
	v_or_b32_e32 v173, 48, v131
	v_or_b32_e32 v174, 49, v131
	v_or_b32_e32 v175, 50, v131
	v_or_b32_e32 v176, 51, v131
	v_or_b32_e32 v177, 56, v131
	v_or_b32_e32 v178, 57, v131
	v_or_b32_e32 v179, 58, v131
	v_or_b32_e32 v180, 59, v131
	v_or_b32_e32 v181, 64, v131
	v_or_b32_e32 v182, 0x41, v131
	v_or_b32_e32 v183, 0x42, v131
	v_or_b32_e32 v184, 0x43, v131
	v_or_b32_e32 v185, 0x48, v131
	v_or_b32_e32 v186, 0x49, v131
	v_or_b32_e32 v187, 0x4a, v131
	v_or_b32_e32 v188, 0x4b, v131
	v_or_b32_e32 v189, 0x50, v131
	v_or_b32_e32 v190, 0x51, v131
	v_or_b32_e32 v191, 0x52, v131
	v_or_b32_e32 v192, 0x53, v131
	v_or_b32_e32 v193, 0x58, v131
	v_or_b32_e32 v194, 0x59, v131
	v_or_b32_e32 v195, 0x5a, v131
	v_or_b32_e32 v196, 0x5b, v131
	v_or_b32_e32 v198, 0x60, v131
	v_or_b32_e32 v199, 0x61, v131
	v_or_b32_e32 v201, 0x62, v131
	v_or_b32_e32 v202, 0x63, v131
	v_or_b32_e32 v203, 0x68, v131
	v_or_b32_e32 v204, 0x69, v131
	v_or_b32_e32 v205, 0x6a, v131
	v_or_b32_e32 v206, 0x6b, v131
	v_or_b32_e32 v207, 0x70, v131
	v_or_b32_e32 v208, 0x71, v131
	v_or_b32_e32 v209, 0x72, v131
	v_or_b32_e32 v210, 0x73, v131
	v_or_b32_e32 v211, 0x78, v131
	v_or_b32_e32 v212, 0x79, v131
	v_or_b32_e32 v213, 0x7a, v131
	v_or_b32_e32 v214, 0x7b, v131
	s_movk_i32 s38, 0xff00
	v_lshlrev_b32_e32 v134, 1, v130
	s_movk_i32 s40, 0x110
	s_movk_i32 s41, 0x1000
	s_mov_b32 s42, 0x42fe0000
	s_mov_b32 s43, 0x40c0c00
	s_movk_i32 s44, 0xff80
	s_mov_b32 s45, 0xff61b1e6
	v_add_u32_e32 v215, s2, v1
	s_mov_b32 s46, 0
	s_mov_b32 s47, s58
	s_branch .LBB0_1207
